# attention-phase weight-copy stores at agent scope (sc1): the fp8 copies leave the XCD L2 instead of displacing K/V lines
# speedup vs baseline: 1.0007x; 1.0007x over previous
; #define GAS __attribute__((address_space(1)))
; #define LAS __attribute__((address_space(3)))
; #define LDS_WAIT() asm volatile("s_waitcnt lgkmcnt(0)" ::: "memory")
; __device__ __forceinline__ void t64_finish(const f32x4 (&tv)[16], unsigned char* dst, int ldd, int f8, LAS unsigned char* scr, int lane) {
;     const int g = lane >> 4, i16 = lane & 15;
; #pragma unroll
;     for (int i = 0; i < 16; ++i) { v2u w; w.x = cvt_pk_bf16(tv[i].x, tv[i].y); w.y = cvt_pk_bf16(tv[i].z, tv[i].w); *(LAS v2u*)(scr + (8 * i + (lane >> 3)) * 64 + 8 * (lane & 7)) = w; }
;     LDS_WAIT(); asm volatile("" ::: "memory");
;     const int q = i16 >> 2, pp = i16 & 3;
;     bf16x8 o[8];
; #pragma unroll
;     for (int jj = 0; jj < 8; ++jj) { const int c = 4 * jj + g, nb = c & 1, kg = c >> 1;
;         LAS unsigned char* ra = scr + (8 * kg + q) * 64 + 32 * nb + 8 * pp;
;         const s16x4 lo = __builtin_bit_cast(s16x4, __builtin_amdgcn_ds_read_tr16_b64_v4i16((LAS s16x4*)ra));
;         const s16x4 hi = __builtin_bit_cast(s16x4, __builtin_amdgcn_ds_read_tr16_b64_v4i16((LAS s16x4*)(ra + 4 * 64)));
;         o[jj] = __builtin_shufflevector(lo, hi, 0, 1, 2, 3, 4, 5, 6, 7); }
;     LDS_WAIT(); asm volatile("" ::: "memory");
; #pragma unroll
;     for (int jj = 0; jj < 8; ++jj) { const int c = 4 * jj + g, nb = c & 1, kg = c >> 1; const int n = 16 * nb + i16;
;         *(LAS bf16x8*)(scr + n * 256 + 16 * (kg ^ (n & 15))) = o[jj]; }
;     LDS_WAIT(); asm volatile("" ::: "memory");
;     const int rr = lane >> 3, cc = lane & 7;
; #pragma unroll
;     for (int it = 0; it < 4; ++it) { const int n = 8 * it + rr;
;         const v4u v0 = *(const LAS v4u*)(scr + n * 256 + 16 * ((2 * cc) ^ (n & 15))), v1 = *(const LAS v4u*)(scr + n * 256 + 16 * ((2 * cc + 1) ^ (n & 15)));
;         if (f8) { v4u o4; o4.x = pk4_fp8(bf_lo(v0.x) * W8_SCALE, bf_hi(v0.x) * W8_SCALE, bf_lo(v0.y) * W8_SCALE, bf_hi(v0.y) * W8_SCALE);
;             o4.y = pk4_fp8(bf_lo(v0.z) * W8_SCALE, bf_hi(v0.z) * W8_SCALE, bf_lo(v0.w) * W8_SCALE, bf_hi(v0.w) * W8_SCALE);
;             o4.z = pk4_fp8(bf_lo(v1.x) * W8_SCALE, bf_hi(v1.x) * W8_SCALE, bf_lo(v1.y) * W8_SCALE, bf_hi(v1.y) * W8_SCALE);
;             o4.w = pk4_fp8(bf_lo(v1.z) * W8_SCALE, bf_hi(v1.z) * W8_SCALE, bf_lo(v1.w) * W8_SCALE, bf_hi(v1.w) * W8_SCALE);
;             __builtin_nontemporal_store(o4, (GAS v4u*)(dst + (size_t)n * ldd + 16 * cc)); }
.LBB0_245:
	v_cvt_pk_bf16_f32 v132, v50, v51
	v_cvt_pk_bf16_f32 v133, v52, v53
	ds_write_b64 v1, v[132:133]
	v_cvt_pk_bf16_f32 v132, v62, v63
	v_cvt_pk_bf16_f32 v133, v64, v65
	ds_write_b64 v1, v[132:133] offset:512
	v_cvt_pk_bf16_f32 v132, v74, v75
	v_cvt_pk_bf16_f32 v133, v76, v77
	ds_write_b64 v1, v[132:133] offset:1024
	v_cvt_pk_bf16_f32 v132, v78, v79
	v_cvt_pk_bf16_f32 v133, v80, v81
	ds_write_b64 v1, v[132:133] offset:1536
	v_cvt_pk_bf16_f32 v132, v82, v83
	v_cvt_pk_bf16_f32 v133, v84, v85
	ds_write_b64 v1, v[132:133] offset:2048
	v_cvt_pk_bf16_f32 v132, v86, v87
	v_cvt_pk_bf16_f32 v133, v88, v89
	ds_write_b64 v1, v[132:133] offset:2560
	v_cvt_pk_bf16_f32 v132, v90, v91
	v_cvt_pk_bf16_f32 v133, v92, v93
	ds_write_b64 v1, v[132:133] offset:3072
	v_cvt_pk_bf16_f32 v132, v94, v95
	v_cvt_pk_bf16_f32 v133, v96, v97
	ds_write_b64 v1, v[132:133] offset:3584
	v_cvt_pk_bf16_f32 v132, v98, v99
	v_cvt_pk_bf16_f32 v133, v100, v101
	ds_write_b64 v1, v[132:133] offset:4096
	v_cvt_pk_bf16_f32 v132, v102, v103
	v_cvt_pk_bf16_f32 v133, v104, v105
	ds_write_b64 v1, v[132:133] offset:4608
	v_cvt_pk_bf16_f32 v132, v106, v107
	v_cvt_pk_bf16_f32 v133, v108, v109
	ds_write_b64 v1, v[132:133] offset:5120
	v_cvt_pk_bf16_f32 v132, v110, v111
	v_cvt_pk_bf16_f32 v133, v112, v113
	ds_write_b64 v1, v[132:133] offset:5632
	v_cvt_pk_bf16_f32 v132, v114, v115
	v_cvt_pk_bf16_f32 v133, v116, v117
	ds_write_b64 v1, v[132:133] offset:6144
	v_cvt_pk_bf16_f32 v132, v118, v119
	v_cvt_pk_bf16_f32 v133, v120, v121
	ds_write_b64 v1, v[132:133] offset:6656
	v_cvt_pk_bf16_f32 v132, v122, v123
	v_cvt_pk_bf16_f32 v133, v124, v125
	ds_write_b64 v1, v[132:133] offset:7168
	v_cvt_pk_bf16_f32 v132, v126, v127
	v_cvt_pk_bf16_f32 v133, v128, v129
	ds_write_b64 v1, v[132:133] offset:7680
	s_waitcnt lgkmcnt(0)
	ds_read_b64_tr_b16 v[152:153], v134
	ds_read_b64_tr_b16 v[154:155], v134 offset:256
	ds_read_b64_tr_b16 v[172:173], v134 offset:1024
	ds_read_b64_tr_b16 v[174:175], v134 offset:1280
	ds_read_b64_tr_b16 v[176:177], v134 offset:2048
	ds_read_b64_tr_b16 v[178:179], v134 offset:2304
	ds_read_b64_tr_b16 v[180:181], v134 offset:3072
	ds_read_b64_tr_b16 v[182:183], v134 offset:3328
	ds_read_b64_tr_b16 v[184:185], v134 offset:4096
	ds_read_b64_tr_b16 v[186:187], v134 offset:4352
	ds_read_b64_tr_b16 v[188:189], v134 offset:5120
	ds_read_b64_tr_b16 v[190:191], v134 offset:5376
	ds_read_b64_tr_b16 v[192:193], v134 offset:6144
	ds_read_b64_tr_b16 v[194:195], v134 offset:6400
	ds_read_b64_tr_b16 v[224:225], v134 offset:7168
	ds_read_b64_tr_b16 v[226:227], v134 offset:7424
	s_waitcnt lgkmcnt(0)
	s_waitcnt lgkmcnt(14)
	ds_write_b128 v135, v[152:155]
	s_waitcnt lgkmcnt(13)
	ds_write_b128 v136, v[172:175]
	s_waitcnt lgkmcnt(12)
	ds_write_b128 v137, v[176:179]
	s_waitcnt lgkmcnt(11)
	ds_write_b128 v138, v[180:183]
	s_waitcnt lgkmcnt(10)
	ds_write_b128 v139, v[184:187]
	s_waitcnt lgkmcnt(9)
	ds_write_b128 v140, v[188:191]
	s_waitcnt lgkmcnt(8)
	ds_write_b128 v141, v[192:195]
	s_waitcnt lgkmcnt(7)
	ds_write_b128 v142, v[224:227]
	s_waitcnt lgkmcnt(0)
	ds_read_b128 v[134:137], v143
	ds_read_b128 v[138:141], v144
	v_lshl_add_u64 v[132:133], s[22:23], 0, v[160:161]
	s_waitcnt lgkmcnt(1)
	v_lshlrev_b32_e32 v1, 16, v134
	v_and_b32_e32 v131, 0xffff0000, v134
	v_mul_f32_e32 v1, 0x42800000, v1
	v_mul_f32_e32 v131, 0x42800000, v131
	v_mov_b32_e32 v134, v171
	v_cvt_pk_fp8_f32 v134, v1, v131
	v_lshlrev_b32_e32 v142, 16, v135
	v_and_b32_e32 v131, 0xffff0000, v135
	v_mul_f32_e32 v1, 0x42800000, v142
	v_mul_f32_e32 v131, 0x42800000, v131
	v_cvt_pk_fp8_f32 v134, v1, v131 op_sel:[0,0,1]
	v_lshlrev_b32_e32 v1, 16, v136
	v_and_b32_e32 v131, 0xffff0000, v136
	v_mul_f32_e32 v1, 0x42800000, v1
	v_mul_f32_e32 v131, 0x42800000, v131
	v_mov_b32_e32 v135, v171
	v_cvt_pk_fp8_f32 v135, v1, v131
	v_lshlrev_b32_e32 v136, 16, v137
	v_and_b32_e32 v131, 0xffff0000, v137
	v_mul_f32_e32 v1, 0x42800000, v136
	v_mul_f32_e32 v131, 0x42800000, v131
	v_cvt_pk_fp8_f32 v135, v1, v131 op_sel:[0,0,1]
	s_waitcnt lgkmcnt(0)
	v_lshlrev_b32_e32 v1, 16, v138
	v_and_b32_e32 v131, 0xffff0000, v138
	v_mul_f32_e32 v1, 0x42800000, v1
	v_mul_f32_e32 v131, 0x42800000, v131
	v_mov_b32_e32 v136, v171
	v_cvt_pk_fp8_f32 v136, v1, v131
	v_lshlrev_b32_e32 v137, 16, v139
	v_and_b32_e32 v131, 0xffff0000, v139
	v_mul_f32_e32 v1, 0x42800000, v137
	v_mul_f32_e32 v131, 0x42800000, v131
	v_cvt_pk_fp8_f32 v136, v1, v131 op_sel:[0,0,1]
	v_lshlrev_b32_e32 v1, 16, v140
	v_and_b32_e32 v131, 0xffff0000, v140
	v_mul_f32_e32 v1, 0x42800000, v1
	v_mul_f32_e32 v131, 0x42800000, v131
	v_mov_b32_e32 v137, v171
	v_cvt_pk_fp8_f32 v137, v1, v131
	v_lshlrev_b32_e32 v138, 16, v141
	v_and_b32_e32 v131, 0xffff0000, v141
	v_mul_f32_e32 v1, 0x42800000, v138
	v_mul_f32_e32 v131, 0x42800000, v131
	ds_read_b128 v[138:141], v145
	v_cvt_pk_fp8_f32 v137, v1, v131 op_sel:[0,0,1]
	v_mad_u64_u32 v[142:143], s[44:45], s64, v158, v[132:133]
	global_store_dwordx4 v[142:143], v[134:137], off sc1
	ds_read_b128 v[134:137], v146
	s_waitcnt lgkmcnt(1)
; #define GAS __attribute__((address_space(1)))
; #define LAS __attribute__((address_space(3)))
; __device__ __forceinline__ unsigned pk4_fp8(float a, float b, float c, float d) { int p = 0; p = __builtin_amdgcn_cvt_pk_fp8_f32(a, b, p, false); p = __builtin_amdgcn_cvt_pk_fp8_f32(c, d, p, true); return (unsigned)p; }
; __device__ __forceinline__ void t64_finish(const f32x4 (&tv)[16], unsigned char* dst, int ldd, int f8, LAS unsigned char* scr, int lane) {
;     ...
;     const int rr = lane >> 3, cc = lane & 7;
; #pragma unroll
;     for (int it = 0; it < 4; ++it) { const int n = 8 * it + rr;
;         const v4u v0 = *(const LAS v4u*)(scr + n * 256 + 16 * ((2 * cc) ^ (n & 15))), v1 = *(const LAS v4u*)(scr + n * 256 + 16 * ((2 * cc + 1) ^ (n & 15)));
;         if (f8) { v4u o4; o4.x = pk4_fp8(bf_lo(v0.x) * W8_SCALE, bf_hi(v0.x) * W8_SCALE, bf_lo(v0.y) * W8_SCALE, bf_hi(v0.y) * W8_SCALE);
;             o4.y = pk4_fp8(bf_lo(v0.z) * W8_SCALE, bf_hi(v0.z) * W8_SCALE, bf_lo(v0.w) * W8_SCALE, bf_hi(v0.w) * W8_SCALE);
;             o4.z = pk4_fp8(bf_lo(v1.x) * W8_SCALE, bf_hi(v1.x) * W8_SCALE, bf_lo(v1.y) * W8_SCALE, bf_hi(v1.y) * W8_SCALE);
;             o4.w = pk4_fp8(bf_lo(v1.z) * W8_SCALE, bf_hi(v1.z) * W8_SCALE, bf_lo(v1.w) * W8_SCALE, bf_hi(v1.w) * W8_SCALE);
;             __builtin_nontemporal_store(o4, (GAS v4u*)(dst + (size_t)n * ldd + 16 * cc)); }
;         else { *(GAS v4u*)(dst + (size_t)n * ldd + 32 * cc) = v0; *(GAS v4u*)(dst + (size_t)n * ldd + 32 * cc + 16) = v1; } }
	v_lshlrev_b32_e32 v1, 16, v138
	v_and_b32_e32 v131, 0xffff0000, v138
	v_mul_f32_e32 v1, 0x42800000, v1
	v_mul_f32_e32 v131, 0x42800000, v131
	v_mov_b32_e32 v138, v171
	v_cvt_pk_fp8_f32 v138, v1, v131
	v_lshlrev_b32_e32 v142, 16, v139
	v_and_b32_e32 v131, 0xffff0000, v139
	v_mul_f32_e32 v1, 0x42800000, v142
	v_mul_f32_e32 v131, 0x42800000, v131
	v_cvt_pk_fp8_f32 v138, v1, v131 op_sel:[0,0,1]
	v_lshlrev_b32_e32 v1, 16, v140
	v_and_b32_e32 v131, 0xffff0000, v140
	v_mul_f32_e32 v1, 0x42800000, v1
	v_mul_f32_e32 v131, 0x42800000, v131
	v_mov_b32_e32 v139, v171
	v_cvt_pk_fp8_f32 v139, v1, v131
	v_lshlrev_b32_e32 v140, 16, v141
	v_and_b32_e32 v131, 0xffff0000, v141
	v_mul_f32_e32 v1, 0x42800000, v140
	v_mul_f32_e32 v131, 0x42800000, v131
	v_cvt_pk_fp8_f32 v139, v1, v131 op_sel:[0,0,1]
	s_waitcnt lgkmcnt(0)
	v_lshlrev_b32_e32 v1, 16, v134
	v_and_b32_e32 v131, 0xffff0000, v134
	v_mul_f32_e32 v1, 0x42800000, v1
	v_mul_f32_e32 v131, 0x42800000, v131
	v_mov_b32_e32 v140, v171
	v_cvt_pk_fp8_f32 v140, v1, v131
	v_lshlrev_b32_e32 v134, 16, v135
	v_and_b32_e32 v131, 0xffff0000, v135
	v_mul_f32_e32 v1, 0x42800000, v134
	v_mul_f32_e32 v131, 0x42800000, v131
	v_cvt_pk_fp8_f32 v140, v1, v131 op_sel:[0,0,1]
	v_lshlrev_b32_e32 v1, 16, v136
	v_and_b32_e32 v131, 0xffff0000, v136
	v_mul_f32_e32 v1, 0x42800000, v1
	v_mul_f32_e32 v131, 0x42800000, v131
	v_mov_b32_e32 v141, v171
	v_cvt_pk_fp8_f32 v141, v1, v131
	v_lshlrev_b32_e32 v134, 16, v137
	v_and_b32_e32 v131, 0xffff0000, v137
	v_mul_f32_e32 v1, 0x42800000, v134
	v_mul_f32_e32 v131, 0x42800000, v131
	ds_read_b128 v[134:137], v147
	v_cvt_pk_fp8_f32 v141, v1, v131 op_sel:[0,0,1]
	v_mad_u64_u32 v[142:143], s[44:45], s64, v162, v[132:133]
	global_store_dwordx4 v[142:143], v[138:141], off sc1
	ds_read_b128 v[138:141], v148
	s_waitcnt lgkmcnt(1)
	v_lshlrev_b32_e32 v1, 16, v134
	v_and_b32_e32 v131, 0xffff0000, v134
	v_mul_f32_e32 v1, 0x42800000, v1
	v_mul_f32_e32 v131, 0x42800000, v131
	v_mov_b32_e32 v134, v171
	v_cvt_pk_fp8_f32 v134, v1, v131
	v_lshlrev_b32_e32 v142, 16, v135
	v_and_b32_e32 v131, 0xffff0000, v135
	v_mul_f32_e32 v1, 0x42800000, v142
	v_mul_f32_e32 v131, 0x42800000, v131
	v_cvt_pk_fp8_f32 v134, v1, v131 op_sel:[0,0,1]
	v_lshlrev_b32_e32 v1, 16, v136
	v_and_b32_e32 v131, 0xffff0000, v136
	v_mul_f32_e32 v1, 0x42800000, v1
	v_mul_f32_e32 v131, 0x42800000, v131
	v_mov_b32_e32 v135, v171
	v_cvt_pk_fp8_f32 v135, v1, v131
	v_lshlrev_b32_e32 v136, 16, v137
	v_and_b32_e32 v131, 0xffff0000, v137
	v_mul_f32_e32 v1, 0x42800000, v136
	v_mul_f32_e32 v131, 0x42800000, v131
	v_cvt_pk_fp8_f32 v135, v1, v131 op_sel:[0,0,1]
	s_waitcnt lgkmcnt(0)
	v_lshlrev_b32_e32 v1, 16, v138
	v_and_b32_e32 v131, 0xffff0000, v138
	v_mul_f32_e32 v1, 0x42800000, v1
	v_mul_f32_e32 v131, 0x42800000, v131
	v_mov_b32_e32 v136, v171
	v_cvt_pk_fp8_f32 v136, v1, v131
	v_lshlrev_b32_e32 v137, 16, v139
	v_and_b32_e32 v131, 0xffff0000, v139
	v_mul_f32_e32 v1, 0x42800000, v137
	v_mul_f32_e32 v131, 0x42800000, v131
	v_cvt_pk_fp8_f32 v136, v1, v131 op_sel:[0,0,1]
	v_lshlrev_b32_e32 v1, 16, v140
	v_and_b32_e32 v131, 0xffff0000, v140
	v_lshlrev_b32_e32 v137, 16, v141
	v_mul_f32_e32 v1, 0x42800000, v1
	v_mul_f32_e32 v131, 0x42800000, v131
	v_mul_f32_e32 v142, 0x42800000, v137
	v_mov_b32_e32 v137, v171
	v_cvt_pk_fp8_f32 v137, v1, v131
	v_and_b32_e32 v1, 0xffff0000, v141
	ds_read_b128 v[138:141], v149
	v_mul_f32_e32 v1, 0x42800000, v1
	v_cvt_pk_fp8_f32 v137, v142, v1 op_sel:[0,0,1]
	ds_read_b128 v[142:145], v150
	v_mad_u64_u32 v[146:147], s[44:45], s64, v164, v[132:133]
	s_waitcnt lgkmcnt(1)
	v_lshlrev_b32_e32 v1, 16, v138
	v_and_b32_e32 v131, 0xffff0000, v138
	v_mul_f32_e32 v1, 0x42800000, v1
	v_mul_f32_e32 v131, 0x42800000, v131
	v_mov_b32_e32 v138, v171
	v_cvt_pk_fp8_f32 v138, v1, v131
	v_lshlrev_b32_e32 v148, 16, v139
	v_and_b32_e32 v131, 0xffff0000, v139
	v_mul_f32_e32 v1, 0x42800000, v148
	v_mul_f32_e32 v131, 0x42800000, v131
	v_cvt_pk_fp8_f32 v138, v1, v131 op_sel:[0,0,1]
	v_lshlrev_b32_e32 v1, 16, v140
	v_and_b32_e32 v131, 0xffff0000, v140
	v_mul_f32_e32 v1, 0x42800000, v1
	v_mul_f32_e32 v131, 0x42800000, v131
	v_mov_b32_e32 v139, v171
	v_cvt_pk_fp8_f32 v139, v1, v131
	v_lshlrev_b32_e32 v140, 16, v141
	v_and_b32_e32 v131, 0xffff0000, v141
	v_mul_f32_e32 v1, 0x42800000, v140
	v_mul_f32_e32 v131, 0x42800000, v131
	v_cvt_pk_fp8_f32 v139, v1, v131 op_sel:[0,0,1]
	s_waitcnt lgkmcnt(0)
	v_lshlrev_b32_e32 v1, 16, v142
	v_and_b32_e32 v131, 0xffff0000, v142
	v_mul_f32_e32 v1, 0x42800000, v1
	v_mul_f32_e32 v131, 0x42800000, v131
	v_mov_b32_e32 v140, v171
	v_cvt_pk_fp8_f32 v140, v1, v131
	v_lshlrev_b32_e32 v141, 16, v143
	v_and_b32_e32 v131, 0xffff0000, v143
	v_mul_f32_e32 v1, 0x42800000, v141
	v_mul_f32_e32 v131, 0x42800000, v131
	v_cvt_pk_fp8_f32 v140, v1, v131 op_sel:[0,0,1]
	v_lshlrev_b32_e32 v1, 16, v144
	v_and_b32_e32 v131, 0xffff0000, v144
	v_mul_f32_e32 v1, 0x42800000, v1
	v_mul_f32_e32 v131, 0x42800000, v131
	v_mov_b32_e32 v141, v171
	v_cvt_pk_fp8_f32 v141, v1, v131
	v_lshlrev_b32_e32 v142, 16, v145
	v_and_b32_e32 v131, 0xffff0000, v145
	v_mul_f32_e32 v1, 0x42800000, v142
	v_mul_f32_e32 v131, 0x42800000, v131
	v_cvt_pk_fp8_f32 v141, v1, v131 op_sel:[0,0,1]
	v_mad_u64_u32 v[132:133], s[44:45], s64, v166, v[132:133]
	global_store_dwordx4 v[146:147], v[134:137], off sc1
	global_store_dwordx4 v[132:133], v[138:141], off sc1
	s_waitcnt lgkmcnt(0)

; #define GAS __attribute__((address_space(1)))
; #define LAS __attribute__((address_space(3)))
; #define LDS_WAIT() asm volatile("s_waitcnt lgkmcnt(0)" ::: "memory")
; __device__ __forceinline__ void t64_finish(const f32x4 (&tv)[16], unsigned char* dst, int ldd, int f8, LAS unsigned char* scr, int lane) {
;     const int g = lane >> 4, i16 = lane & 15;
; #pragma unroll
;     for (int i = 0; i < 16; ++i) { v2u w; w.x = cvt_pk_bf16(tv[i].x, tv[i].y); w.y = cvt_pk_bf16(tv[i].z, tv[i].w); *(LAS v2u*)(scr + (8 * i + (lane >> 3)) * 64 + 8 * (lane & 7)) = w; }
;     LDS_WAIT(); asm volatile("" ::: "memory");
;     const int q = i16 >> 2, pp = i16 & 3;
;     bf16x8 o[8];
; #pragma unroll
;     for (int jj = 0; jj < 8; ++jj) { const int c = 4 * jj + g, nb = c & 1, kg = c >> 1;
;         LAS unsigned char* ra = scr + (8 * kg + q) * 64 + 32 * nb + 8 * pp;
;         const s16x4 lo = __builtin_bit_cast(s16x4, __builtin_amdgcn_ds_read_tr16_b64_v4i16((LAS s16x4*)ra));
;         const s16x4 hi = __builtin_bit_cast(s16x4, __builtin_amdgcn_ds_read_tr16_b64_v4i16((LAS s16x4*)(ra + 4 * 64)));
;         o[jj] = __builtin_shufflevector(lo, hi, 0, 1, 2, 3, 4, 5, 6, 7); }
;     LDS_WAIT(); asm volatile("" ::: "memory");
; #pragma unroll
;     for (int jj = 0; jj < 8; ++jj) { const int c = 4 * jj + g, nb = c & 1, kg = c >> 1; const int n = 16 * nb + i16;
;         *(LAS bf16x8*)(scr + n * 256 + 16 * (kg ^ (n & 15))) = o[jj]; }
;     LDS_WAIT(); asm volatile("" ::: "memory");
;     const int rr = lane >> 3, cc = lane & 7;
; #pragma unroll
;     for (int it = 0; it < 4; ++it) { const int n = 8 * it + rr;
;         const v4u v0 = *(const LAS v4u*)(scr + n * 256 + 16 * ((2 * cc) ^ (n & 15))), v1 = *(const LAS v4u*)(scr + n * 256 + 16 * ((2 * cc + 1) ^ (n & 15)));
;         if (f8) { v4u o4; o4.x = pk4_fp8(bf_lo(v0.x) * W8_SCALE, bf_hi(v0.x) * W8_SCALE, bf_lo(v0.y) * W8_SCALE, bf_hi(v0.y) * W8_SCALE);
;             o4.y = pk4_fp8(bf_lo(v0.z) * W8_SCALE, bf_hi(v0.z) * W8_SCALE, bf_lo(v0.w) * W8_SCALE, bf_hi(v0.w) * W8_SCALE);
;             o4.z = pk4_fp8(bf_lo(v1.x) * W8_SCALE, bf_hi(v1.x) * W8_SCALE, bf_lo(v1.y) * W8_SCALE, bf_hi(v1.y) * W8_SCALE);
;             o4.w = pk4_fp8(bf_lo(v1.z) * W8_SCALE, bf_hi(v1.z) * W8_SCALE, bf_lo(v1.w) * W8_SCALE, bf_hi(v1.w) * W8_SCALE);
;             __builtin_nontemporal_store(o4, (GAS v4u*)(dst + (size_t)n * ldd + 16 * cc)); }
.LcvwP2a_a:
	v_cvt_pk_bf16_f32 v132, v2, v3
	v_cvt_pk_bf16_f32 v133, v4, v5
	v_add_u32_e32 v1, v163, v165
	ds_write_b64 v1, v[132:133]
	v_cvt_pk_bf16_f32 v132, v6, v7
	v_cvt_pk_bf16_f32 v133, v8, v9
	ds_write_b64 v1, v[132:133] offset:512
	v_cvt_pk_bf16_f32 v132, v10, v11
	v_cvt_pk_bf16_f32 v133, v12, v13
	ds_write_b64 v1, v[132:133] offset:1024
	v_cvt_pk_bf16_f32 v132, v14, v15
	v_cvt_pk_bf16_f32 v133, v16, v17
	ds_write_b64 v1, v[132:133] offset:1536
	v_cvt_pk_bf16_f32 v132, v18, v19
	v_cvt_pk_bf16_f32 v133, v20, v21
	ds_write_b64 v1, v[132:133] offset:2048
	v_cvt_pk_bf16_f32 v132, v22, v23
	v_cvt_pk_bf16_f32 v133, v24, v25
	ds_write_b64 v1, v[132:133] offset:2560
	v_cvt_pk_bf16_f32 v132, v26, v27
	v_cvt_pk_bf16_f32 v133, v28, v29
	ds_write_b64 v1, v[132:133] offset:3072
	v_cvt_pk_bf16_f32 v132, v30, v31
	v_cvt_pk_bf16_f32 v133, v32, v33
	ds_write_b64 v1, v[132:133] offset:3584
	v_cvt_pk_bf16_f32 v132, v34, v35
	v_cvt_pk_bf16_f32 v133, v36, v37
	ds_write_b64 v1, v[132:133] offset:4096
	v_cvt_pk_bf16_f32 v132, v38, v39
	v_cvt_pk_bf16_f32 v133, v40, v41
	ds_write_b64 v1, v[132:133] offset:4608
	v_cvt_pk_bf16_f32 v132, v42, v43
	v_cvt_pk_bf16_f32 v133, v44, v45
	ds_write_b64 v1, v[132:133] offset:5120
	v_cvt_pk_bf16_f32 v132, v46, v47
	v_cvt_pk_bf16_f32 v133, v48, v49
	ds_write_b64 v1, v[132:133] offset:5632
	v_cvt_pk_bf16_f32 v132, v54, v55
	v_cvt_pk_bf16_f32 v133, v56, v57
	ds_write_b64 v1, v[132:133] offset:6144
	v_cvt_pk_bf16_f32 v132, v58, v59
	v_cvt_pk_bf16_f32 v133, v60, v61
	ds_write_b64 v1, v[132:133] offset:6656
	v_cvt_pk_bf16_f32 v132, v66, v67
	v_cvt_pk_bf16_f32 v133, v68, v69
	ds_write_b64 v1, v[132:133] offset:7168
	v_cvt_pk_bf16_f32 v132, v70, v71
	v_cvt_pk_bf16_f32 v133, v72, v73
	ds_write_b64 v1, v[132:133] offset:7680
	s_waitcnt lgkmcnt(0)
	v_add_u32_e32 v134, v167, v169
	ds_read_b64_tr_b16 v[136:137], v134
	ds_read_b64_tr_b16 v[138:139], v134 offset:256
	ds_read_b64_tr_b16 v[140:141], v134 offset:1024
	ds_read_b64_tr_b16 v[142:143], v134 offset:1280
	ds_read_b64_tr_b16 v[144:145], v134 offset:2048
	ds_read_b64_tr_b16 v[146:147], v134 offset:2304
	ds_read_b64_tr_b16 v[148:149], v134 offset:3072
	ds_read_b64_tr_b16 v[150:151], v134 offset:3328
	ds_read_b64_tr_b16 v[152:153], v134 offset:4096
	ds_read_b64_tr_b16 v[154:155], v134 offset:4352
	ds_read_b64_tr_b16 v[172:173], v134 offset:5120
	ds_read_b64_tr_b16 v[174:175], v134 offset:5376
	ds_read_b64_tr_b16 v[176:177], v134 offset:6144
	ds_read_b64_tr_b16 v[178:179], v134 offset:6400
	ds_read_b64_tr_b16 v[180:181], v134 offset:7168
	ds_read_b64_tr_b16 v[182:183], v134 offset:7424
	s_waitcnt lgkmcnt(0)
	v_add_u32_e32 v135, v204, v205
	s_waitcnt lgkmcnt(14)
	ds_write_b128 v135, v[136:139]
	v_add_u32_e32 v136, v204, v206
	s_waitcnt lgkmcnt(13)
	ds_write_b128 v136, v[140:143]
	v_add_u32_e32 v137, v204, v207
	v_add_u32_e32 v138, v204, v208
	v_add_u32_e32 v139, v204, v209
	v_add_u32_e32 v140, v204, v210
	v_add_u32_e32 v141, v204, v211
	v_add_u32_e32 v142, v204, v212
	s_waitcnt lgkmcnt(12)
	ds_write_b128 v137, v[144:147]
	s_waitcnt lgkmcnt(11)
	ds_write_b128 v138, v[148:151]
	s_waitcnt lgkmcnt(10)
	ds_write_b128 v139, v[152:155]
	s_waitcnt lgkmcnt(9)
	ds_write_b128 v140, v[172:175]
	s_waitcnt lgkmcnt(8)
	ds_write_b128 v141, v[176:179]
	s_waitcnt lgkmcnt(7)
	ds_write_b128 v142, v[180:183]
	s_waitcnt lgkmcnt(0)
	v_add_u32_e32 v143, v213, v214
	ds_read_b128 v[146:149], v143
	v_add_u32_e32 v144, v213, v215
	ds_read_b128 v[150:153], v144
	v_lshl_add_u64 v[132:133], s[6:7], 0, v[160:161]
	v_mad_u64_u32 v[180:181], s[62:63], s84, v164, v[132:133]
	s_waitcnt lgkmcnt(1)
	v_lshlrev_b32_e32 v131, 16, v146
	v_and_b32_e32 v145, 0xffff0000, v146
	v_mul_f32_e32 v131, 0x42800000, v131
	v_mul_f32_e32 v145, 0x42800000, v145
	v_mov_b32_e32 v146, v171
	v_cvt_pk_fp8_f32 v146, v131, v145
	v_lshlrev_b32_e32 v154, 16, v147
	v_and_b32_e32 v145, 0xffff0000, v147
	v_mul_f32_e32 v131, 0x42800000, v154
	v_mul_f32_e32 v145, 0x42800000, v145
	v_cvt_pk_fp8_f32 v146, v131, v145 op_sel:[0,0,1]
	v_lshlrev_b32_e32 v131, 16, v148
	v_and_b32_e32 v145, 0xffff0000, v148
	v_mul_f32_e32 v131, 0x42800000, v131
	v_mul_f32_e32 v145, 0x42800000, v145
	v_mov_b32_e32 v147, v171
	v_cvt_pk_fp8_f32 v147, v131, v145
	v_lshlrev_b32_e32 v148, 16, v149
	v_and_b32_e32 v145, 0xffff0000, v149
	v_mul_f32_e32 v131, 0x42800000, v148
	v_mul_f32_e32 v145, 0x42800000, v145
	v_cvt_pk_fp8_f32 v147, v131, v145 op_sel:[0,0,1]
	s_waitcnt lgkmcnt(0)
	v_lshlrev_b32_e32 v131, 16, v150
	v_and_b32_e32 v145, 0xffff0000, v150
	v_mul_f32_e32 v131, 0x42800000, v131
	v_mul_f32_e32 v145, 0x42800000, v145
	v_mov_b32_e32 v148, v171
	v_cvt_pk_fp8_f32 v148, v131, v145
	v_lshlrev_b32_e32 v149, 16, v151
	v_and_b32_e32 v145, 0xffff0000, v151
	v_mul_f32_e32 v131, 0x42800000, v149
	v_mul_f32_e32 v145, 0x42800000, v145
	v_cvt_pk_fp8_f32 v148, v131, v145 op_sel:[0,0,1]
	v_lshlrev_b32_e32 v131, 16, v152
	v_and_b32_e32 v145, 0xffff0000, v152
	v_mul_f32_e32 v131, 0x42800000, v131
	v_mul_f32_e32 v145, 0x42800000, v145
	v_mov_b32_e32 v149, v171
	v_cvt_pk_fp8_f32 v149, v131, v145
	v_lshlrev_b32_e32 v150, 16, v153
	v_and_b32_e32 v145, 0xffff0000, v153
	v_mul_f32_e32 v131, 0x42800000, v150
	v_mul_f32_e32 v145, 0x42800000, v145
	v_cvt_pk_fp8_f32 v149, v131, v145 op_sel:[0,0,1]
	v_add_u32_e32 v145, v216, v217
	ds_read_b128 v[150:153], v145
	v_mad_u64_u32 v[154:155], s[62:63], s84, v158, v[132:133]
	global_store_dwordx4 v[154:155], v[146:149], off sc1
	s_andn2_b64 vcc, exec, s[44:45]
	s_nop 0
	v_add_u32_e32 v146, v216, v218
	ds_read_b128 v[172:175], v146
	s_waitcnt lgkmcnt(1)
; #define GAS __attribute__((address_space(1)))
; #define LAS __attribute__((address_space(3)))
; __device__ __forceinline__ unsigned pk4_fp8(float a, float b, float c, float d) { int p = 0; p = __builtin_amdgcn_cvt_pk_fp8_f32(a, b, p, false); p = __builtin_amdgcn_cvt_pk_fp8_f32(c, d, p, true); return (unsigned)p; }
; __device__ __forceinline__ void t64_finish(const f32x4 (&tv)[16], unsigned char* dst, int ldd, int f8, LAS unsigned char* scr, int lane) {
;     ...
;     const int rr = lane >> 3, cc = lane & 7;
; #pragma unroll
;     for (int it = 0; it < 4; ++it) { const int n = 8 * it + rr;
;         const v4u v0 = *(const LAS v4u*)(scr + n * 256 + 16 * ((2 * cc) ^ (n & 15))), v1 = *(const LAS v4u*)(scr + n * 256 + 16 * ((2 * cc + 1) ^ (n & 15)));
;         if (f8) { v4u o4; o4.x = pk4_fp8(bf_lo(v0.x) * W8_SCALE, bf_hi(v0.x) * W8_SCALE, bf_lo(v0.y) * W8_SCALE, bf_hi(v0.y) * W8_SCALE);
;             o4.y = pk4_fp8(bf_lo(v0.z) * W8_SCALE, bf_hi(v0.z) * W8_SCALE, bf_lo(v0.w) * W8_SCALE, bf_hi(v0.w) * W8_SCALE);
;             o4.z = pk4_fp8(bf_lo(v1.x) * W8_SCALE, bf_hi(v1.x) * W8_SCALE, bf_lo(v1.y) * W8_SCALE, bf_hi(v1.y) * W8_SCALE);
;             o4.w = pk4_fp8(bf_lo(v1.z) * W8_SCALE, bf_hi(v1.z) * W8_SCALE, bf_lo(v1.w) * W8_SCALE, bf_hi(v1.w) * W8_SCALE);
;             __builtin_nontemporal_store(o4, (GAS v4u*)(dst + (size_t)n * ldd + 16 * cc)); }
;         else { *(GAS v4u*)(dst + (size_t)n * ldd + 32 * cc) = v0; *(GAS v4u*)(dst + (size_t)n * ldd + 32 * cc + 16) = v1; } }
; __device__ __forceinline__ XItem xitem(const float* w_gate, const float* w_up, const float* w_down, bf16* BTGU, bf16* BTD, int r) {
;     ...
;     { const int per = (DFF / 128) * (DM / 32); const int e = r / per, r3 = r % per; const int nblk = DM / 32, kb = r3 / nblk, nb = r3 % nblk;
;         it.src = w_down + (size_t)e * DFF * DM + (size_t)(128 * kb) * DM + 32 * nb; it.ldw = DM; it.dst = (unsigned char*)BTD + ((size_t)e * DM + 32 * nb) * DFF + 128 * kb; it.ldd = DFF; it.f8 = 1; return it; }
	v_lshlrev_b32_e32 v131, 16, v150
	v_and_b32_e32 v147, 0xffff0000, v150
	v_mul_f32_e32 v131, 0x42800000, v131
	v_mul_f32_e32 v147, 0x42800000, v147
	v_mov_b32_e32 v148, v171
	v_cvt_pk_fp8_f32 v148, v131, v147
	v_lshlrev_b32_e32 v149, 16, v151
	v_and_b32_e32 v147, 0xffff0000, v151
	v_mul_f32_e32 v131, 0x42800000, v149
	v_mul_f32_e32 v147, 0x42800000, v147
	v_cvt_pk_fp8_f32 v148, v131, v147 op_sel:[0,0,1]
	v_lshlrev_b32_e32 v131, 16, v152
	v_and_b32_e32 v147, 0xffff0000, v152
	v_mul_f32_e32 v131, 0x42800000, v131
	v_mul_f32_e32 v147, 0x42800000, v147
	v_mov_b32_e32 v149, v171
	v_cvt_pk_fp8_f32 v149, v131, v147
	v_lshlrev_b32_e32 v150, 16, v153
	v_and_b32_e32 v147, 0xffff0000, v153
	v_mul_f32_e32 v131, 0x42800000, v150
	v_mul_f32_e32 v147, 0x42800000, v147
	v_cvt_pk_fp8_f32 v149, v131, v147 op_sel:[0,0,1]
	s_waitcnt lgkmcnt(0)
	v_lshlrev_b32_e32 v131, 16, v172
	v_and_b32_e32 v147, 0xffff0000, v172
	v_mul_f32_e32 v131, 0x42800000, v131
	v_mul_f32_e32 v147, 0x42800000, v147
	v_mov_b32_e32 v150, v171
	v_cvt_pk_fp8_f32 v150, v131, v147
	v_lshlrev_b32_e32 v151, 16, v173
	v_and_b32_e32 v147, 0xffff0000, v173
	v_mul_f32_e32 v131, 0x42800000, v151
	v_mul_f32_e32 v147, 0x42800000, v147
	v_cvt_pk_fp8_f32 v150, v131, v147 op_sel:[0,0,1]
	v_lshlrev_b32_e32 v131, 16, v174
	v_and_b32_e32 v147, 0xffff0000, v174
	v_mul_f32_e32 v131, 0x42800000, v131
	v_mul_f32_e32 v147, 0x42800000, v147
	v_mov_b32_e32 v151, v171
	v_cvt_pk_fp8_f32 v151, v131, v147
	v_lshlrev_b32_e32 v152, 16, v175
	v_and_b32_e32 v147, 0xffff0000, v175
	v_mul_f32_e32 v131, 0x42800000, v152
	v_mul_f32_e32 v147, 0x42800000, v147
	v_cvt_pk_fp8_f32 v151, v131, v147 op_sel:[0,0,1]
	v_add_u32_e32 v147, v219, v214
	ds_read_b128 v[152:155], v147
	v_mad_u64_u32 v[172:173], s[62:63], s84, v162, v[132:133]
	global_store_dwordx4 v[172:173], v[148:151], off sc1
	v_mad_u64_u32 v[132:133], s[62:63], s84, v166, v[132:133]
	s_nop 0
	v_add_u32_e32 v148, v219, v215
	ds_read_b128 v[172:175], v148
	s_waitcnt lgkmcnt(1)
	v_lshlrev_b32_e32 v131, 16, v152
	v_and_b32_e32 v149, 0xffff0000, v152
	v_mul_f32_e32 v131, 0x42800000, v131
	v_mul_f32_e32 v149, 0x42800000, v149
	v_mov_b32_e32 v152, v171
	v_cvt_pk_fp8_f32 v152, v131, v149
	v_lshlrev_b32_e32 v150, 16, v153
	v_and_b32_e32 v149, 0xffff0000, v153
	v_mul_f32_e32 v131, 0x42800000, v150
	v_mul_f32_e32 v149, 0x42800000, v149
	v_cvt_pk_fp8_f32 v152, v131, v149 op_sel:[0,0,1]
	v_lshlrev_b32_e32 v131, 16, v154
	v_and_b32_e32 v149, 0xffff0000, v154
	v_mul_f32_e32 v131, 0x42800000, v131
	v_mul_f32_e32 v149, 0x42800000, v149
	v_mov_b32_e32 v153, v171
	v_cvt_pk_fp8_f32 v153, v131, v149
	v_lshlrev_b32_e32 v150, 16, v155
	v_and_b32_e32 v149, 0xffff0000, v155
	v_mul_f32_e32 v131, 0x42800000, v150
	v_mul_f32_e32 v149, 0x42800000, v149
	v_cvt_pk_fp8_f32 v153, v131, v149 op_sel:[0,0,1]
	s_waitcnt lgkmcnt(0)
	v_lshlrev_b32_e32 v131, 16, v172
	v_and_b32_e32 v149, 0xffff0000, v172
	v_mul_f32_e32 v131, 0x42800000, v131
	v_mul_f32_e32 v149, 0x42800000, v149
	v_mov_b32_e32 v154, v171
	v_cvt_pk_fp8_f32 v154, v131, v149
	v_lshlrev_b32_e32 v150, 16, v173
	v_and_b32_e32 v149, 0xffff0000, v173
	v_mul_f32_e32 v131, 0x42800000, v150
	v_mul_f32_e32 v149, 0x42800000, v149
	v_cvt_pk_fp8_f32 v154, v131, v149 op_sel:[0,0,1]
	v_lshlrev_b32_e32 v131, 16, v174
	v_and_b32_e32 v149, 0xffff0000, v174
	v_mul_f32_e32 v131, 0x42800000, v131
	v_mul_f32_e32 v149, 0x42800000, v149
	v_mov_b32_e32 v155, v171
	v_cvt_pk_fp8_f32 v155, v131, v149
	v_lshlrev_b32_e32 v150, 16, v175
	v_and_b32_e32 v149, 0xffff0000, v175
	v_mul_f32_e32 v131, 0x42800000, v150
	v_mul_f32_e32 v149, 0x42800000, v149
	v_cvt_pk_fp8_f32 v155, v131, v149 op_sel:[0,0,1]
	v_add_u32_e32 v149, v220, v221
	ds_read_b128 v[172:175], v149
	v_add_u32_e32 v150, v220, v222
	ds_read_b128 v[176:179], v150
	global_store_dwordx4 v[180:181], v[152:155], off sc1
	s_waitcnt lgkmcnt(1)
	v_lshlrev_b32_e32 v131, 16, v172
	v_and_b32_e32 v151, 0xffff0000, v172
	v_mul_f32_e32 v131, 0x42800000, v131
	v_mul_f32_e32 v151, 0x42800000, v151
	v_mov_b32_e32 v172, v171
	v_cvt_pk_fp8_f32 v172, v131, v151
	v_lshlrev_b32_e32 v170, 16, v173
	v_and_b32_e32 v151, 0xffff0000, v173
	v_mul_f32_e32 v131, 0x42800000, v170
	v_mul_f32_e32 v151, 0x42800000, v151
	v_cvt_pk_fp8_f32 v172, v131, v151 op_sel:[0,0,1]
	v_lshlrev_b32_e32 v131, 16, v174
	v_and_b32_e32 v151, 0xffff0000, v174
	v_mul_f32_e32 v131, 0x42800000, v131
	v_mul_f32_e32 v151, 0x42800000, v151
	v_mov_b32_e32 v173, v171
	v_cvt_pk_fp8_f32 v173, v131, v151
	v_lshlrev_b32_e32 v170, 16, v175
	v_and_b32_e32 v151, 0xffff0000, v175
	v_mul_f32_e32 v131, 0x42800000, v170
	v_mul_f32_e32 v151, 0x42800000, v151
	v_cvt_pk_fp8_f32 v173, v131, v151 op_sel:[0,0,1]
	s_waitcnt lgkmcnt(0)
	v_lshlrev_b32_e32 v131, 16, v176
	v_and_b32_e32 v151, 0xffff0000, v176
	v_mul_f32_e32 v131, 0x42800000, v131
	v_mul_f32_e32 v151, 0x42800000, v151
	v_mov_b32_e32 v174, v171
	v_cvt_pk_fp8_f32 v174, v131, v151
	v_lshlrev_b32_e32 v170, 16, v177
	v_and_b32_e32 v151, 0xffff0000, v177
	v_mul_f32_e32 v131, 0x42800000, v170
	v_mul_f32_e32 v151, 0x42800000, v151
	v_cvt_pk_fp8_f32 v174, v131, v151 op_sel:[0,0,1]
	v_lshlrev_b32_e32 v131, 16, v178
	v_and_b32_e32 v151, 0xffff0000, v178
	v_mul_f32_e32 v131, 0x42800000, v131
	v_mul_f32_e32 v151, 0x42800000, v151
	v_mov_b32_e32 v175, v171
	v_cvt_pk_fp8_f32 v175, v131, v151
	v_lshlrev_b32_e32 v170, 16, v179
	v_and_b32_e32 v151, 0xffff0000, v179
	v_mul_f32_e32 v131, 0x42800000, v170
	v_mul_f32_e32 v151, 0x42800000, v151
	v_cvt_pk_fp8_f32 v175, v131, v151 op_sel:[0,0,1]
	global_store_dwordx4 v[132:133], v[172:175], off sc1
	s_waitcnt lgkmcnt(0)
	s_cbranch_vccnz .LBB0_246
	s_add_i32 s65, s57, 0x8001
	s_cmp_ge_i32 s65, s21
	s_cbranch_scc1 .LcvwP2a_b
	s_cmpk_gt_i32 s33, 0x7ffd
	s_mov_b64 s[62:63], -1
	s_cbranch_scc0 .LBB0_258
	s_add_i32 s0, s57, 1
	s_lshr_b32 s0, s0, 9
	s_lshl_b64 s[6:7], s[0:1], 23
	s_add_u32 s6, s58, s6
	s_addc_u32 s7, s59, s7
	s_and_b32 s33, s52, 0x380
	s_lshl_b32 s44, s33, 13
	s_add_u32 s6, s6, s44
	s_addc_u32 s7, s7, 0
	s_and_b32 s54, s56, 0x7e0
	s_lshl_b32 s44, s54, 2
	s_add_u32 s44, s6, s44
	s_addc_u32 s45, s7, 0
	s_lshl_b64 s[6:7], s[0:1], 21
	s_lshl_b32 s0, s54, 10
	s_add_u32 s6, s70, s6
	s_addc_u32 s7, s71, s7
	s_add_u32 s0, s6, s0
	s_addc_u32 s7, s7, 0
	s_add_u32 s6, s0, s33
	s_addc_u32 s7, s7, 0
	s_mov_b64 s[62:63], 0

; #define GAS __attribute__((address_space(1)))
; #define LAS __attribute__((address_space(3)))
; #define LDS_WAIT() asm volatile("s_waitcnt lgkmcnt(0)" ::: "memory")
; __device__ __forceinline__ void t64_finish(const f32x4 (&tv)[16], unsigned char* dst, int ldd, int f8, LAS unsigned char* scr, int lane) {
;     const int g = lane >> 4, i16 = lane & 15;
; #pragma unroll
;     for (int i = 0; i < 16; ++i) { v2u w; w.x = cvt_pk_bf16(tv[i].x, tv[i].y); w.y = cvt_pk_bf16(tv[i].z, tv[i].w); *(LAS v2u*)(scr + (8 * i + (lane >> 3)) * 64 + 8 * (lane & 7)) = w; }
;     LDS_WAIT(); asm volatile("" ::: "memory");
;     const int q = i16 >> 2, pp = i16 & 3;
;     bf16x8 o[8];
; #pragma unroll
;     for (int jj = 0; jj < 8; ++jj) { const int c = 4 * jj + g, nb = c & 1, kg = c >> 1;
;         LAS unsigned char* ra = scr + (8 * kg + q) * 64 + 32 * nb + 8 * pp;
;         const s16x4 lo = __builtin_bit_cast(s16x4, __builtin_amdgcn_ds_read_tr16_b64_v4i16((LAS s16x4*)ra));
;         const s16x4 hi = __builtin_bit_cast(s16x4, __builtin_amdgcn_ds_read_tr16_b64_v4i16((LAS s16x4*)(ra + 4 * 64)));
;         o[jj] = __builtin_shufflevector(lo, hi, 0, 1, 2, 3, 4, 5, 6, 7); }
;     LDS_WAIT(); asm volatile("" ::: "memory");
; #pragma unroll
;     for (int jj = 0; jj < 8; ++jj) { const int c = 4 * jj + g, nb = c & 1, kg = c >> 1; const int n = 16 * nb + i16;
;         *(LAS bf16x8*)(scr + n * 256 + 16 * (kg ^ (n & 15))) = o[jj]; }
;     LDS_WAIT(); asm volatile("" ::: "memory");
;     const int rr = lane >> 3, cc = lane & 7;
; #pragma unroll
;     for (int it = 0; it < 4; ++it) { const int n = 8 * it + rr;
;         const v4u v0 = *(const LAS v4u*)(scr + n * 256 + 16 * ((2 * cc) ^ (n & 15))), v1 = *(const LAS v4u*)(scr + n * 256 + 16 * ((2 * cc + 1) ^ (n & 15)));
;         if (f8) { v4u o4; o4.x = pk4_fp8(bf_lo(v0.x) * W8_SCALE, bf_hi(v0.x) * W8_SCALE, bf_lo(v0.y) * W8_SCALE, bf_hi(v0.y) * W8_SCALE);
;             o4.y = pk4_fp8(bf_lo(v0.z) * W8_SCALE, bf_hi(v0.z) * W8_SCALE, bf_lo(v0.w) * W8_SCALE, bf_hi(v0.w) * W8_SCALE);
;             o4.z = pk4_fp8(bf_lo(v1.x) * W8_SCALE, bf_hi(v1.x) * W8_SCALE, bf_lo(v1.y) * W8_SCALE, bf_hi(v1.y) * W8_SCALE);
;             o4.w = pk4_fp8(bf_lo(v1.z) * W8_SCALE, bf_hi(v1.z) * W8_SCALE, bf_lo(v1.w) * W8_SCALE, bf_hi(v1.w) * W8_SCALE);
;             __builtin_nontemporal_store(o4, (GAS v4u*)(dst + (size_t)n * ldd + 16 * cc)); }
.LBB0_269:
	v_cvt_pk_bf16_f32 v132, v48, v49
	v_cvt_pk_bf16_f32 v133, v50, v51
	ds_write_b64 v134, v[132:133]
	v_cvt_pk_bf16_f32 v132, v60, v61
	v_cvt_pk_bf16_f32 v133, v62, v63
	ds_write_b64 v134, v[132:133] offset:512
	v_cvt_pk_bf16_f32 v132, v72, v73
	v_cvt_pk_bf16_f32 v133, v74, v75
	ds_write_b64 v134, v[132:133] offset:1024
	v_cvt_pk_bf16_f32 v132, v76, v77
	v_cvt_pk_bf16_f32 v133, v78, v79
	ds_write_b64 v134, v[132:133] offset:1536
	v_cvt_pk_bf16_f32 v132, v80, v81
	v_cvt_pk_bf16_f32 v133, v82, v83
	ds_write_b64 v134, v[132:133] offset:2048
	v_cvt_pk_bf16_f32 v132, v84, v85
	v_cvt_pk_bf16_f32 v133, v86, v87
	ds_write_b64 v134, v[132:133] offset:2560
	v_cvt_pk_bf16_f32 v132, v88, v89
	v_cvt_pk_bf16_f32 v133, v90, v91
	ds_write_b64 v134, v[132:133] offset:3072
	v_cvt_pk_bf16_f32 v132, v92, v93
	v_cvt_pk_bf16_f32 v133, v94, v95
	ds_write_b64 v134, v[132:133] offset:3584
	v_cvt_pk_bf16_f32 v132, v96, v97
	v_cvt_pk_bf16_f32 v133, v98, v99
	ds_write_b64 v134, v[132:133] offset:4096
	v_cvt_pk_bf16_f32 v132, v100, v101
	v_cvt_pk_bf16_f32 v133, v102, v103
	ds_write_b64 v134, v[132:133] offset:4608
	v_cvt_pk_bf16_f32 v132, v104, v105
	v_cvt_pk_bf16_f32 v133, v106, v107
	ds_write_b64 v134, v[132:133] offset:5120
	v_cvt_pk_bf16_f32 v132, v108, v109
	v_cvt_pk_bf16_f32 v133, v110, v111
	ds_write_b64 v134, v[132:133] offset:5632
	v_cvt_pk_bf16_f32 v132, v112, v113
	v_cvt_pk_bf16_f32 v133, v114, v115
	ds_write_b64 v134, v[132:133] offset:6144
	v_cvt_pk_bf16_f32 v132, v116, v117
	v_cvt_pk_bf16_f32 v133, v118, v119
	ds_write_b64 v134, v[132:133] offset:6656
	v_cvt_pk_bf16_f32 v132, v120, v121
	v_cvt_pk_bf16_f32 v133, v122, v123
	ds_write_b64 v134, v[132:133] offset:7168
	v_cvt_pk_bf16_f32 v132, v124, v125
	v_cvt_pk_bf16_f32 v133, v126, v127
	ds_write_b64 v134, v[132:133] offset:7680
	s_waitcnt lgkmcnt(0)
	ds_read_b64_tr_b16 v[152:153], v135
	ds_read_b64_tr_b16 v[154:155], v135 offset:256
	ds_read_b64_tr_b16 v[170:171], v135 offset:1024
	ds_read_b64_tr_b16 v[172:173], v135 offset:1280
	ds_read_b64_tr_b16 v[174:175], v135 offset:2048
	ds_read_b64_tr_b16 v[176:177], v135 offset:2304
	ds_read_b64_tr_b16 v[178:179], v135 offset:3072
	ds_read_b64_tr_b16 v[180:181], v135 offset:3328
	ds_read_b64_tr_b16 v[182:183], v135 offset:4096
	ds_read_b64_tr_b16 v[184:185], v135 offset:4352
	ds_read_b64_tr_b16 v[186:187], v135 offset:5120
	ds_read_b64_tr_b16 v[188:189], v135 offset:5376
	ds_read_b64_tr_b16 v[190:191], v135 offset:6144
	ds_read_b64_tr_b16 v[192:193], v135 offset:6400
	ds_read_b64_tr_b16 v[132:133], v135 offset:7168
	ds_read_b64_tr_b16 v[134:135], v135 offset:7424
	s_waitcnt lgkmcnt(0)
	s_waitcnt lgkmcnt(14)
	ds_write_b128 v136, v[152:155]
	s_waitcnt lgkmcnt(13)
	ds_write_b128 v137, v[170:173]
	s_waitcnt lgkmcnt(12)
	ds_write_b128 v138, v[174:177]
	s_waitcnt lgkmcnt(11)
	ds_write_b128 v139, v[178:181]
	s_waitcnt lgkmcnt(10)
	ds_write_b128 v140, v[182:185]
	s_waitcnt lgkmcnt(9)
	ds_write_b128 v141, v[186:189]
	s_waitcnt lgkmcnt(8)
	ds_write_b128 v142, v[190:193]
	s_waitcnt lgkmcnt(7)
	ds_write_b128 v143, v[132:135]
	s_waitcnt lgkmcnt(0)
	ds_read_b128 v[134:137], v144
	ds_read_b128 v[138:141], v145
	v_lshl_add_u64 v[132:133], s[16:17], 0, v[160:161]
	s_waitcnt lgkmcnt(1)
	v_lshlrev_b32_e32 v128, 16, v134
	v_and_b32_e32 v131, 0xffff0000, v134
	v_mul_f32_e32 v128, 0x42800000, v128
	v_mul_f32_e32 v131, 0x42800000, v131
	v_mov_b32_e32 v134, v129
	v_cvt_pk_fp8_f32 v134, v128, v131
	v_lshlrev_b32_e32 v142, 16, v135
	v_and_b32_e32 v131, 0xffff0000, v135
	v_mul_f32_e32 v128, 0x42800000, v142
	v_mul_f32_e32 v131, 0x42800000, v131
	v_cvt_pk_fp8_f32 v134, v128, v131 op_sel:[0,0,1]
	v_lshlrev_b32_e32 v128, 16, v136
	v_and_b32_e32 v131, 0xffff0000, v136
	v_mul_f32_e32 v128, 0x42800000, v128
	v_mul_f32_e32 v131, 0x42800000, v131
	v_mov_b32_e32 v135, v129
	v_cvt_pk_fp8_f32 v135, v128, v131
	v_lshlrev_b32_e32 v136, 16, v137
	v_and_b32_e32 v131, 0xffff0000, v137
	v_mul_f32_e32 v128, 0x42800000, v136
	v_mul_f32_e32 v131, 0x42800000, v131
	v_cvt_pk_fp8_f32 v135, v128, v131 op_sel:[0,0,1]
	s_waitcnt lgkmcnt(0)
	v_lshlrev_b32_e32 v128, 16, v138
	v_and_b32_e32 v131, 0xffff0000, v138
	v_mul_f32_e32 v128, 0x42800000, v128
	v_mul_f32_e32 v131, 0x42800000, v131
	v_mov_b32_e32 v136, v129
	v_cvt_pk_fp8_f32 v136, v128, v131
	v_lshlrev_b32_e32 v137, 16, v139
	v_and_b32_e32 v131, 0xffff0000, v139
	v_mul_f32_e32 v128, 0x42800000, v137
	v_mul_f32_e32 v131, 0x42800000, v131
	v_cvt_pk_fp8_f32 v136, v128, v131 op_sel:[0,0,1]
	v_lshlrev_b32_e32 v128, 16, v140
	v_and_b32_e32 v131, 0xffff0000, v140
	v_mul_f32_e32 v128, 0x42800000, v128
	v_mul_f32_e32 v131, 0x42800000, v131
	v_mov_b32_e32 v137, v129
	v_cvt_pk_fp8_f32 v137, v128, v131
	v_lshlrev_b32_e32 v138, 16, v141
	v_and_b32_e32 v131, 0xffff0000, v141
	v_mul_f32_e32 v128, 0x42800000, v138
	v_mul_f32_e32 v131, 0x42800000, v131
	ds_read_b128 v[138:141], v146
	v_cvt_pk_fp8_f32 v137, v128, v131 op_sel:[0,0,1]
	v_mad_u64_u32 v[142:143], s[20:21], s40, v158, v[132:133]
	global_store_dwordx4 v[142:143], v[134:137], off sc1
	ds_read_b128 v[134:137], v147
	s_waitcnt lgkmcnt(1)
; #define GAS __attribute__((address_space(1)))
; #define LAS __attribute__((address_space(3)))
; __device__ __forceinline__ unsigned pk4_fp8(float a, float b, float c, float d) { int p = 0; p = __builtin_amdgcn_cvt_pk_fp8_f32(a, b, p, false); p = __builtin_amdgcn_cvt_pk_fp8_f32(c, d, p, true); return (unsigned)p; }
; __device__ __forceinline__ void t64_finish(const f32x4 (&tv)[16], unsigned char* dst, int ldd, int f8, LAS unsigned char* scr, int lane) {
;     ...
;     const int rr = lane >> 3, cc = lane & 7;
; #pragma unroll
;     for (int it = 0; it < 4; ++it) { const int n = 8 * it + rr;
;         const v4u v0 = *(const LAS v4u*)(scr + n * 256 + 16 * ((2 * cc) ^ (n & 15))), v1 = *(const LAS v4u*)(scr + n * 256 + 16 * ((2 * cc + 1) ^ (n & 15)));
;         if (f8) { v4u o4; o4.x = pk4_fp8(bf_lo(v0.x) * W8_SCALE, bf_hi(v0.x) * W8_SCALE, bf_lo(v0.y) * W8_SCALE, bf_hi(v0.y) * W8_SCALE);
;             o4.y = pk4_fp8(bf_lo(v0.z) * W8_SCALE, bf_hi(v0.z) * W8_SCALE, bf_lo(v0.w) * W8_SCALE, bf_hi(v0.w) * W8_SCALE);
;             o4.z = pk4_fp8(bf_lo(v1.x) * W8_SCALE, bf_hi(v1.x) * W8_SCALE, bf_lo(v1.y) * W8_SCALE, bf_hi(v1.y) * W8_SCALE);
;             o4.w = pk4_fp8(bf_lo(v1.z) * W8_SCALE, bf_hi(v1.z) * W8_SCALE, bf_lo(v1.w) * W8_SCALE, bf_hi(v1.w) * W8_SCALE);
;             __builtin_nontemporal_store(o4, (GAS v4u*)(dst + (size_t)n * ldd + 16 * cc)); }
;         else { *(GAS v4u*)(dst + (size_t)n * ldd + 32 * cc) = v0; *(GAS v4u*)(dst + (size_t)n * ldd + 32 * cc + 16) = v1; } }
	v_lshlrev_b32_e32 v128, 16, v138
	v_and_b32_e32 v131, 0xffff0000, v138
	v_mul_f32_e32 v128, 0x42800000, v128
	v_mul_f32_e32 v131, 0x42800000, v131
	v_mov_b32_e32 v138, v129
	v_cvt_pk_fp8_f32 v138, v128, v131
	v_lshlrev_b32_e32 v142, 16, v139
	v_and_b32_e32 v131, 0xffff0000, v139
	v_mul_f32_e32 v128, 0x42800000, v142
	v_mul_f32_e32 v131, 0x42800000, v131
	v_cvt_pk_fp8_f32 v138, v128, v131 op_sel:[0,0,1]
	v_lshlrev_b32_e32 v128, 16, v140
	v_and_b32_e32 v131, 0xffff0000, v140
	v_mul_f32_e32 v128, 0x42800000, v128
	v_mul_f32_e32 v131, 0x42800000, v131
	v_mov_b32_e32 v139, v129
	v_cvt_pk_fp8_f32 v139, v128, v131
	v_lshlrev_b32_e32 v140, 16, v141
	v_and_b32_e32 v131, 0xffff0000, v141
	v_mul_f32_e32 v128, 0x42800000, v140
	v_mul_f32_e32 v131, 0x42800000, v131
	v_cvt_pk_fp8_f32 v139, v128, v131 op_sel:[0,0,1]
	s_waitcnt lgkmcnt(0)
	v_lshlrev_b32_e32 v128, 16, v134
	v_and_b32_e32 v131, 0xffff0000, v134
	v_mul_f32_e32 v128, 0x42800000, v128
	v_mul_f32_e32 v131, 0x42800000, v131
	v_mov_b32_e32 v140, v129
	v_cvt_pk_fp8_f32 v140, v128, v131
	v_lshlrev_b32_e32 v134, 16, v135
	v_and_b32_e32 v131, 0xffff0000, v135
	v_mul_f32_e32 v128, 0x42800000, v134
	v_mul_f32_e32 v131, 0x42800000, v131
	v_cvt_pk_fp8_f32 v140, v128, v131 op_sel:[0,0,1]
	v_lshlrev_b32_e32 v128, 16, v136
	v_and_b32_e32 v131, 0xffff0000, v136
	v_mul_f32_e32 v128, 0x42800000, v128
	v_mul_f32_e32 v131, 0x42800000, v131
	v_mov_b32_e32 v141, v129
	v_cvt_pk_fp8_f32 v141, v128, v131
	v_lshlrev_b32_e32 v134, 16, v137
	v_and_b32_e32 v131, 0xffff0000, v137
	v_mul_f32_e32 v128, 0x42800000, v134
	v_mul_f32_e32 v131, 0x42800000, v131
	ds_read_b128 v[134:137], v148
	v_cvt_pk_fp8_f32 v141, v128, v131 op_sel:[0,0,1]
	v_mad_u64_u32 v[142:143], s[20:21], s40, v162, v[132:133]
	v_mad_u64_u32 v[146:147], s[20:21], s40, v164, v[132:133]
	global_store_dwordx4 v[142:143], v[138:141], off sc1
	ds_read_b128 v[138:141], v149
	s_waitcnt lgkmcnt(1)
	v_lshlrev_b32_e32 v128, 16, v134
	v_and_b32_e32 v131, 0xffff0000, v134
	v_mul_f32_e32 v128, 0x42800000, v128
	v_mul_f32_e32 v131, 0x42800000, v131
	v_mov_b32_e32 v134, v129
	v_cvt_pk_fp8_f32 v134, v128, v131
	v_lshlrev_b32_e32 v142, 16, v135
	v_and_b32_e32 v131, 0xffff0000, v135
	v_mul_f32_e32 v128, 0x42800000, v142
	v_mul_f32_e32 v131, 0x42800000, v131
	v_cvt_pk_fp8_f32 v134, v128, v131 op_sel:[0,0,1]
	v_lshlrev_b32_e32 v128, 16, v136
	v_and_b32_e32 v131, 0xffff0000, v136
	v_mul_f32_e32 v128, 0x42800000, v128
	v_mul_f32_e32 v131, 0x42800000, v131
	v_mov_b32_e32 v135, v129
	v_cvt_pk_fp8_f32 v135, v128, v131
	v_lshlrev_b32_e32 v136, 16, v137
	v_and_b32_e32 v131, 0xffff0000, v137
	v_mul_f32_e32 v128, 0x42800000, v136
	v_mul_f32_e32 v131, 0x42800000, v131
	v_cvt_pk_fp8_f32 v135, v128, v131 op_sel:[0,0,1]
	s_waitcnt lgkmcnt(0)
	v_lshlrev_b32_e32 v128, 16, v138
	v_and_b32_e32 v131, 0xffff0000, v138
	v_mul_f32_e32 v128, 0x42800000, v128
	v_mul_f32_e32 v131, 0x42800000, v131
	v_mov_b32_e32 v136, v129
	v_cvt_pk_fp8_f32 v136, v128, v131
	v_lshlrev_b32_e32 v137, 16, v139
	v_and_b32_e32 v131, 0xffff0000, v139
	v_mul_f32_e32 v128, 0x42800000, v137
	v_mul_f32_e32 v131, 0x42800000, v131
	v_cvt_pk_fp8_f32 v136, v128, v131 op_sel:[0,0,1]
	v_lshlrev_b32_e32 v128, 16, v140
	v_and_b32_e32 v131, 0xffff0000, v140
	v_lshlrev_b32_e32 v137, 16, v141
	v_mul_f32_e32 v128, 0x42800000, v128
	v_mul_f32_e32 v131, 0x42800000, v131
	v_mul_f32_e32 v142, 0x42800000, v137
	v_mov_b32_e32 v137, v129
	v_cvt_pk_fp8_f32 v137, v128, v131
	v_and_b32_e32 v128, 0xffff0000, v141
	ds_read_b128 v[138:141], v150
	v_mul_f32_e32 v128, 0x42800000, v128
	v_cvt_pk_fp8_f32 v137, v142, v128 op_sel:[0,0,1]
	ds_read_b128 v[142:145], v151
	v_mad_u64_u32 v[132:133], s[20:21], s40, v166, v[132:133]
	s_waitcnt lgkmcnt(1)
	v_lshlrev_b32_e32 v128, 16, v138
	v_and_b32_e32 v131, 0xffff0000, v138
	v_mul_f32_e32 v128, 0x42800000, v128
	v_mul_f32_e32 v131, 0x42800000, v131
	v_mov_b32_e32 v138, v129
	v_cvt_pk_fp8_f32 v138, v128, v131
	v_lshlrev_b32_e32 v148, 16, v139
	v_and_b32_e32 v131, 0xffff0000, v139
	v_mul_f32_e32 v128, 0x42800000, v148
	v_mul_f32_e32 v131, 0x42800000, v131
	v_cvt_pk_fp8_f32 v138, v128, v131 op_sel:[0,0,1]
	v_lshlrev_b32_e32 v128, 16, v140
	v_and_b32_e32 v131, 0xffff0000, v140
	v_mul_f32_e32 v128, 0x42800000, v128
	v_mul_f32_e32 v131, 0x42800000, v131
	v_mov_b32_e32 v139, v129
	v_cvt_pk_fp8_f32 v139, v128, v131
	v_lshlrev_b32_e32 v140, 16, v141
	v_and_b32_e32 v131, 0xffff0000, v141
	v_mul_f32_e32 v128, 0x42800000, v140
	v_mul_f32_e32 v131, 0x42800000, v131
	v_cvt_pk_fp8_f32 v139, v128, v131 op_sel:[0,0,1]
	s_waitcnt lgkmcnt(0)
	v_lshlrev_b32_e32 v128, 16, v142
	v_and_b32_e32 v131, 0xffff0000, v142
	v_mul_f32_e32 v128, 0x42800000, v128
	v_mul_f32_e32 v131, 0x42800000, v131
	v_mov_b32_e32 v140, v129
	v_cvt_pk_fp8_f32 v140, v128, v131
	v_lshlrev_b32_e32 v141, 16, v143
	v_and_b32_e32 v131, 0xffff0000, v143
	v_mul_f32_e32 v128, 0x42800000, v141
	v_mul_f32_e32 v131, 0x42800000, v131
	v_cvt_pk_fp8_f32 v140, v128, v131 op_sel:[0,0,1]
	v_lshlrev_b32_e32 v128, 16, v144
	v_and_b32_e32 v131, 0xffff0000, v144
	v_mul_f32_e32 v128, 0x42800000, v128
	v_mul_f32_e32 v131, 0x42800000, v131
	v_mov_b32_e32 v141, v129
	v_cvt_pk_fp8_f32 v141, v128, v131
	v_lshlrev_b32_e32 v142, 16, v145
	v_and_b32_e32 v131, 0xffff0000, v145
	v_mul_f32_e32 v128, 0x42800000, v142
	v_mul_f32_e32 v131, 0x42800000, v131
	v_cvt_pk_fp8_f32 v141, v128, v131 op_sel:[0,0,1]
	global_store_dwordx4 v[146:147], v[134:137], off sc1
	global_store_dwordx4 v[132:133], v[138:141], off sc1
	s_waitcnt lgkmcnt(0)

; #define GAS __attribute__((address_space(1)))
; #define LAS __attribute__((address_space(3)))
; #define LDS_WAIT() asm volatile("s_waitcnt lgkmcnt(0)" ::: "memory")
; __device__ __forceinline__ void t64_finish(const f32x4 (&tv)[16], unsigned char* dst, int ldd, int f8, LAS unsigned char* scr, int lane) {
;     const int g = lane >> 4, i16 = lane & 15;
; #pragma unroll
;     for (int i = 0; i < 16; ++i) { v2u w; w.x = cvt_pk_bf16(tv[i].x, tv[i].y); w.y = cvt_pk_bf16(tv[i].z, tv[i].w); *(LAS v2u*)(scr + (8 * i + (lane >> 3)) * 64 + 8 * (lane & 7)) = w; }
;     LDS_WAIT(); asm volatile("" ::: "memory");
;     const int q = i16 >> 2, pp = i16 & 3;
;     bf16x8 o[8];
; #pragma unroll
;     for (int jj = 0; jj < 8; ++jj) { const int c = 4 * jj + g, nb = c & 1, kg = c >> 1;
;         LAS unsigned char* ra = scr + (8 * kg + q) * 64 + 32 * nb + 8 * pp;
;         const s16x4 lo = __builtin_bit_cast(s16x4, __builtin_amdgcn_ds_read_tr16_b64_v4i16((LAS s16x4*)ra));
;         const s16x4 hi = __builtin_bit_cast(s16x4, __builtin_amdgcn_ds_read_tr16_b64_v4i16((LAS s16x4*)(ra + 4 * 64)));
;         o[jj] = __builtin_shufflevector(lo, hi, 0, 1, 2, 3, 4, 5, 6, 7); }
;     LDS_WAIT(); asm volatile("" ::: "memory");
; #pragma unroll
;     for (int jj = 0; jj < 8; ++jj) { const int c = 4 * jj + g, nb = c & 1, kg = c >> 1; const int n = 16 * nb + i16;
;         *(LAS bf16x8*)(scr + n * 256 + 16 * (kg ^ (n & 15))) = o[jj]; }
;     LDS_WAIT(); asm volatile("" ::: "memory");
;     const int rr = lane >> 3, cc = lane & 7;
; #pragma unroll
;     for (int it = 0; it < 4; ++it) { const int n = 8 * it + rr;
;         const v4u v0 = *(const LAS v4u*)(scr + n * 256 + 16 * ((2 * cc) ^ (n & 15))), v1 = *(const LAS v4u*)(scr + n * 256 + 16 * ((2 * cc + 1) ^ (n & 15)));
;         if (f8) { v4u o4; o4.x = pk4_fp8(bf_lo(v0.x) * W8_SCALE, bf_hi(v0.x) * W8_SCALE, bf_lo(v0.y) * W8_SCALE, bf_hi(v0.y) * W8_SCALE);
;             o4.y = pk4_fp8(bf_lo(v0.z) * W8_SCALE, bf_hi(v0.z) * W8_SCALE, bf_lo(v0.w) * W8_SCALE, bf_hi(v0.w) * W8_SCALE);
;             o4.z = pk4_fp8(bf_lo(v1.x) * W8_SCALE, bf_hi(v1.x) * W8_SCALE, bf_lo(v1.y) * W8_SCALE, bf_hi(v1.y) * W8_SCALE);
;             o4.w = pk4_fp8(bf_lo(v1.z) * W8_SCALE, bf_hi(v1.z) * W8_SCALE, bf_lo(v1.w) * W8_SCALE, bf_hi(v1.w) * W8_SCALE);
;             __builtin_nontemporal_store(o4, (GAS v4u*)(dst + (size_t)n * ldd + 16 * cc)); }
.LcvwP2b_a:
	v_cvt_pk_bf16_f32 v132, v0, v1
	v_cvt_pk_bf16_f32 v133, v2, v3
	v_add_u32_e32 v134, v163, v165
	ds_write_b64 v134, v[132:133]
	v_cvt_pk_bf16_f32 v132, v4, v5
	v_cvt_pk_bf16_f32 v133, v6, v7
	ds_write_b64 v134, v[132:133] offset:512
	v_cvt_pk_bf16_f32 v132, v8, v9
	v_cvt_pk_bf16_f32 v133, v10, v11
	ds_write_b64 v134, v[132:133] offset:1024
	v_cvt_pk_bf16_f32 v132, v12, v13
	v_cvt_pk_bf16_f32 v133, v14, v15
	ds_write_b64 v134, v[132:133] offset:1536
	v_cvt_pk_bf16_f32 v132, v16, v17
	v_cvt_pk_bf16_f32 v133, v18, v19
	ds_write_b64 v134, v[132:133] offset:2048
	v_cvt_pk_bf16_f32 v132, v20, v21
	v_cvt_pk_bf16_f32 v133, v22, v23
	ds_write_b64 v134, v[132:133] offset:2560
	v_cvt_pk_bf16_f32 v132, v24, v25
	v_cvt_pk_bf16_f32 v133, v26, v27
	ds_write_b64 v134, v[132:133] offset:3072
	v_cvt_pk_bf16_f32 v132, v28, v29
	v_cvt_pk_bf16_f32 v133, v30, v31
	ds_write_b64 v134, v[132:133] offset:3584
	v_cvt_pk_bf16_f32 v132, v32, v33
	v_cvt_pk_bf16_f32 v133, v34, v35
	ds_write_b64 v134, v[132:133] offset:4096
	v_cvt_pk_bf16_f32 v132, v36, v37
	v_cvt_pk_bf16_f32 v133, v38, v39
	ds_write_b64 v134, v[132:133] offset:4608
	v_cvt_pk_bf16_f32 v132, v40, v41
	v_cvt_pk_bf16_f32 v133, v42, v43
	ds_write_b64 v134, v[132:133] offset:5120
	v_cvt_pk_bf16_f32 v132, v44, v45
	v_cvt_pk_bf16_f32 v133, v46, v47
	ds_write_b64 v134, v[132:133] offset:5632
	v_cvt_pk_bf16_f32 v132, v52, v53
	v_cvt_pk_bf16_f32 v133, v54, v55
	ds_write_b64 v134, v[132:133] offset:6144
	v_cvt_pk_bf16_f32 v132, v56, v57
	v_cvt_pk_bf16_f32 v133, v58, v59
	ds_write_b64 v134, v[132:133] offset:6656
	v_cvt_pk_bf16_f32 v132, v64, v65
	v_cvt_pk_bf16_f32 v133, v66, v67
	ds_write_b64 v134, v[132:133] offset:7168
	v_cvt_pk_bf16_f32 v132, v68, v69
	v_cvt_pk_bf16_f32 v133, v70, v71
	ds_write_b64 v134, v[132:133] offset:7680
	s_waitcnt lgkmcnt(0)
	v_add_u32_e32 v135, v167, v169
	ds_read_b64_tr_b16 v[138:139], v135
	ds_read_b64_tr_b16 v[140:141], v135 offset:256
	ds_read_b64_tr_b16 v[142:143], v135 offset:1024
	ds_read_b64_tr_b16 v[144:145], v135 offset:1280
	ds_read_b64_tr_b16 v[146:147], v135 offset:2048
	ds_read_b64_tr_b16 v[148:149], v135 offset:2304
	ds_read_b64_tr_b16 v[150:151], v135 offset:3072
	ds_read_b64_tr_b16 v[152:153], v135 offset:3328
	ds_read_b64_tr_b16 v[170:171], v135 offset:4096
	ds_read_b64_tr_b16 v[172:173], v135 offset:4352
	ds_read_b64_tr_b16 v[174:175], v135 offset:5120
	ds_read_b64_tr_b16 v[176:177], v135 offset:5376
	ds_read_b64_tr_b16 v[178:179], v135 offset:6144
	ds_read_b64_tr_b16 v[180:181], v135 offset:6400
	ds_read_b64_tr_b16 v[182:183], v135 offset:7168
	ds_read_b64_tr_b16 v[184:185], v135 offset:7424
	s_waitcnt lgkmcnt(0)
	v_add_u32_e32 v136, v204, v205
	v_add_u32_e32 v137, v204, v206
	s_waitcnt lgkmcnt(14)
	ds_write_b128 v136, v[138:141]
	s_waitcnt lgkmcnt(13)
	ds_write_b128 v137, v[142:145]
	v_add_u32_e32 v138, v204, v207
	v_add_u32_e32 v139, v204, v208
	v_add_u32_e32 v140, v204, v209
	v_add_u32_e32 v141, v204, v210
	v_add_u32_e32 v142, v204, v211
	v_add_u32_e32 v143, v204, v212
	s_waitcnt lgkmcnt(12)
	ds_write_b128 v138, v[146:149]
	s_waitcnt lgkmcnt(11)
	ds_write_b128 v139, v[150:153]
	s_waitcnt lgkmcnt(10)
	ds_write_b128 v140, v[170:173]
	s_waitcnt lgkmcnt(9)
	ds_write_b128 v141, v[174:177]
	s_waitcnt lgkmcnt(8)
	ds_write_b128 v142, v[178:181]
	s_waitcnt lgkmcnt(7)
	ds_write_b128 v143, v[182:185]
	s_waitcnt lgkmcnt(0)
	v_add_u32_e32 v144, v213, v214
	ds_read_b128 v[146:149], v144
	v_add_u32_e32 v145, v213, v215
	ds_read_b128 v[150:153], v145
	v_mov_b32_e32 v170, v129
	v_mov_b32_e32 v171, v129
	s_waitcnt lgkmcnt(1)
	v_lshlrev_b32_e32 v128, 16, v146
	v_and_b32_e32 v131, 0xffff0000, v146
	v_mul_f32_e32 v128, 0x42800000, v128
	v_mul_f32_e32 v131, 0x42800000, v131
	v_cvt_pk_fp8_f32 v170, v128, v131
	v_lshlrev_b32_e32 v146, 16, v147
	v_and_b32_e32 v131, 0xffff0000, v147
	v_mul_f32_e32 v128, 0x42800000, v146
	v_mul_f32_e32 v131, 0x42800000, v131
	v_cvt_pk_fp8_f32 v170, v128, v131 op_sel:[0,0,1]
	v_lshlrev_b32_e32 v128, 16, v148
	v_and_b32_e32 v131, 0xffff0000, v148
	v_mul_f32_e32 v128, 0x42800000, v128
	v_mul_f32_e32 v131, 0x42800000, v131
	v_cvt_pk_fp8_f32 v171, v128, v131
	v_lshlrev_b32_e32 v146, 16, v149
	v_and_b32_e32 v131, 0xffff0000, v149
	v_mul_f32_e32 v128, 0x42800000, v146
	v_mul_f32_e32 v131, 0x42800000, v131
	v_cvt_pk_fp8_f32 v171, v128, v131 op_sel:[0,0,1]
	s_waitcnt lgkmcnt(0)
	v_lshlrev_b32_e32 v128, 16, v150
	v_and_b32_e32 v131, 0xffff0000, v150
	v_mul_f32_e32 v128, 0x42800000, v128
	v_mul_f32_e32 v131, 0x42800000, v131
	v_mov_b32_e32 v172, v129
	v_cvt_pk_fp8_f32 v172, v128, v131
	v_lshlrev_b32_e32 v146, 16, v151
	v_and_b32_e32 v131, 0xffff0000, v151
	v_mul_f32_e32 v128, 0x42800000, v146
	v_mul_f32_e32 v131, 0x42800000, v131
	v_cvt_pk_fp8_f32 v172, v128, v131 op_sel:[0,0,1]
	v_lshlrev_b32_e32 v128, 16, v152
	v_and_b32_e32 v131, 0xffff0000, v152
	v_mul_f32_e32 v128, 0x42800000, v128
	v_mul_f32_e32 v131, 0x42800000, v131
	v_mov_b32_e32 v173, v129
	v_cvt_pk_fp8_f32 v173, v128, v131
	v_lshlrev_b32_e32 v146, 16, v153
	v_mul_f32_e32 v128, 0x42800000, v146
	v_and_b32_e32 v131, 0xffff0000, v153
	v_add_u32_e32 v146, v216, v217
	v_mul_f32_e32 v131, 0x42800000, v131
	ds_read_b128 v[148:151], v146
	v_cvt_pk_fp8_f32 v173, v128, v131 op_sel:[0,0,1]
	v_lshl_add_u64 v[132:133], s[6:7], 0, v[160:161]
	v_mad_u64_u32 v[152:153], s[22:23], s45, v158, v[132:133]
	v_add_u32_e32 v147, v216, v218
	global_store_dwordx4 v[152:153], v[170:173], off sc1
	ds_read_b128 v[152:155], v147
	s_waitcnt lgkmcnt(1)
; #define GAS __attribute__((address_space(1)))
; #define LAS __attribute__((address_space(3)))
; __device__ __forceinline__ unsigned pk4_fp8(float a, float b, float c, float d) { int p = 0; p = __builtin_amdgcn_cvt_pk_fp8_f32(a, b, p, false); p = __builtin_amdgcn_cvt_pk_fp8_f32(c, d, p, true); return (unsigned)p; }
; __device__ __forceinline__ void t64_finish(const f32x4 (&tv)[16], unsigned char* dst, int ldd, int f8, LAS unsigned char* scr, int lane) {
;     ...
;     const int rr = lane >> 3, cc = lane & 7;
; #pragma unroll
;     for (int it = 0; it < 4; ++it) { const int n = 8 * it + rr;
;         const v4u v0 = *(const LAS v4u*)(scr + n * 256 + 16 * ((2 * cc) ^ (n & 15))), v1 = *(const LAS v4u*)(scr + n * 256 + 16 * ((2 * cc + 1) ^ (n & 15)));
;         if (f8) { v4u o4; o4.x = pk4_fp8(bf_lo(v0.x) * W8_SCALE, bf_hi(v0.x) * W8_SCALE, bf_lo(v0.y) * W8_SCALE, bf_hi(v0.y) * W8_SCALE);
;             o4.y = pk4_fp8(bf_lo(v0.z) * W8_SCALE, bf_hi(v0.z) * W8_SCALE, bf_lo(v0.w) * W8_SCALE, bf_hi(v0.w) * W8_SCALE);
;             o4.z = pk4_fp8(bf_lo(v1.x) * W8_SCALE, bf_hi(v1.x) * W8_SCALE, bf_lo(v1.y) * W8_SCALE, bf_hi(v1.y) * W8_SCALE);
;             o4.w = pk4_fp8(bf_lo(v1.z) * W8_SCALE, bf_hi(v1.z) * W8_SCALE, bf_lo(v1.w) * W8_SCALE, bf_hi(v1.w) * W8_SCALE);
;             __builtin_nontemporal_store(o4, (GAS v4u*)(dst + (size_t)n * ldd + 16 * cc)); }
;         else { *(GAS v4u*)(dst + (size_t)n * ldd + 32 * cc) = v0; *(GAS v4u*)(dst + (size_t)n * ldd + 32 * cc + 16) = v1; } }
; __device__ __forceinline__ XItem xitem(const float* w_gate, const float* w_up, const float* w_down, bf16* BTGU, bf16* BTD, int r) {
;     ...
;     { const int per = (DFF / 128) * (DM / 32); const int e = r / per, r3 = r % per; const int nblk = DM / 32, kb = r3 / nblk, nb = r3 % nblk;
;         it.src = w_down + (size_t)e * DFF * DM + (size_t)(128 * kb) * DM + 32 * nb; it.ldw = DM; it.dst = (unsigned char*)BTD + ((size_t)e * DM + 32 * nb) * DFF + 128 * kb; it.ldd = DFF; it.f8 = 1; return it; }
	v_lshlrev_b32_e32 v128, 16, v148
	v_and_b32_e32 v131, 0xffff0000, v148
	v_mul_f32_e32 v128, 0x42800000, v128
	v_mul_f32_e32 v131, 0x42800000, v131
	v_mov_b32_e32 v170, v129
	v_cvt_pk_fp8_f32 v170, v128, v131
	v_lshlrev_b32_e32 v148, 16, v149
	v_and_b32_e32 v131, 0xffff0000, v149
	v_mul_f32_e32 v128, 0x42800000, v148
	v_mul_f32_e32 v131, 0x42800000, v131
	v_cvt_pk_fp8_f32 v170, v128, v131 op_sel:[0,0,1]
	v_lshlrev_b32_e32 v128, 16, v150
	v_and_b32_e32 v131, 0xffff0000, v150
	v_mul_f32_e32 v128, 0x42800000, v128
	v_mul_f32_e32 v131, 0x42800000, v131
	v_mov_b32_e32 v171, v129
	v_cvt_pk_fp8_f32 v171, v128, v131
	v_lshlrev_b32_e32 v148, 16, v151
	v_and_b32_e32 v131, 0xffff0000, v151
	v_mul_f32_e32 v128, 0x42800000, v148
	v_mul_f32_e32 v131, 0x42800000, v131
	v_cvt_pk_fp8_f32 v171, v128, v131 op_sel:[0,0,1]
	s_waitcnt lgkmcnt(0)
	v_lshlrev_b32_e32 v128, 16, v152
	v_and_b32_e32 v131, 0xffff0000, v152
	v_mul_f32_e32 v128, 0x42800000, v128
	v_mul_f32_e32 v131, 0x42800000, v131
	v_mov_b32_e32 v172, v129
	v_cvt_pk_fp8_f32 v172, v128, v131
	v_lshlrev_b32_e32 v148, 16, v153
	v_and_b32_e32 v131, 0xffff0000, v153
	v_mul_f32_e32 v128, 0x42800000, v148
	v_mul_f32_e32 v131, 0x42800000, v131
	v_cvt_pk_fp8_f32 v172, v128, v131 op_sel:[0,0,1]
	v_lshlrev_b32_e32 v128, 16, v154
	v_and_b32_e32 v131, 0xffff0000, v154
	v_mul_f32_e32 v128, 0x42800000, v128
	v_mul_f32_e32 v131, 0x42800000, v131
	v_mov_b32_e32 v173, v129
	v_cvt_pk_fp8_f32 v173, v128, v131
	v_lshlrev_b32_e32 v148, 16, v155
	v_mul_f32_e32 v128, 0x42800000, v148
	v_and_b32_e32 v131, 0xffff0000, v155
	v_add_u32_e32 v148, v219, v214
	v_mul_f32_e32 v131, 0x42800000, v131
	ds_read_b128 v[150:153], v148
	v_cvt_pk_fp8_f32 v173, v128, v131 op_sel:[0,0,1]
	v_mad_u64_u32 v[154:155], s[22:23], s45, v162, v[132:133]
	v_add_u32_e32 v149, v219, v215
	global_store_dwordx4 v[154:155], v[170:173], off sc1
	ds_read_b128 v[170:173], v149
	s_waitcnt lgkmcnt(1)
	v_lshlrev_b32_e32 v128, 16, v150
	v_and_b32_e32 v131, 0xffff0000, v150
	v_mul_f32_e32 v128, 0x42800000, v128
	v_mul_f32_e32 v131, 0x42800000, v131
	v_mov_b32_e32 v174, v129
	v_cvt_pk_fp8_f32 v174, v128, v131
	v_lshlrev_b32_e32 v150, 16, v151
	v_and_b32_e32 v131, 0xffff0000, v151
	v_mul_f32_e32 v128, 0x42800000, v150
	v_mul_f32_e32 v131, 0x42800000, v131
	v_cvt_pk_fp8_f32 v174, v128, v131 op_sel:[0,0,1]
	v_lshlrev_b32_e32 v128, 16, v152
	v_and_b32_e32 v131, 0xffff0000, v152
	v_mul_f32_e32 v128, 0x42800000, v128
	v_mul_f32_e32 v131, 0x42800000, v131
	v_mov_b32_e32 v175, v129
	v_cvt_pk_fp8_f32 v175, v128, v131
	v_lshlrev_b32_e32 v150, 16, v153
	v_and_b32_e32 v131, 0xffff0000, v153
	v_mul_f32_e32 v128, 0x42800000, v150
	v_mul_f32_e32 v131, 0x42800000, v131
	v_cvt_pk_fp8_f32 v175, v128, v131 op_sel:[0,0,1]
	s_waitcnt lgkmcnt(0)
	v_lshlrev_b32_e32 v128, 16, v170
	v_and_b32_e32 v131, 0xffff0000, v170
	v_mul_f32_e32 v128, 0x42800000, v128
	v_mul_f32_e32 v131, 0x42800000, v131
	v_mov_b32_e32 v176, v129
	v_cvt_pk_fp8_f32 v176, v128, v131
	v_lshlrev_b32_e32 v150, 16, v171
	v_and_b32_e32 v131, 0xffff0000, v171
	v_mul_f32_e32 v128, 0x42800000, v150
	v_mul_f32_e32 v131, 0x42800000, v131
	v_cvt_pk_fp8_f32 v176, v128, v131 op_sel:[0,0,1]
	v_lshlrev_b32_e32 v128, 16, v172
	v_and_b32_e32 v131, 0xffff0000, v172
	v_mul_f32_e32 v128, 0x42800000, v128
	v_mul_f32_e32 v131, 0x42800000, v131
	v_lshlrev_b32_e32 v150, 16, v173
	v_mov_b32_e32 v177, v129
	v_cvt_pk_fp8_f32 v177, v128, v131
	v_mul_f32_e32 v128, 0x42800000, v150
	v_add_u32_e32 v150, v220, v221
	ds_read_b128 v[152:155], v150
	v_and_b32_e32 v131, 0xffff0000, v173
	v_mul_f32_e32 v131, 0x42800000, v131
	v_add_u32_e32 v151, v220, v222
	v_cvt_pk_fp8_f32 v177, v128, v131 op_sel:[0,0,1]
	ds_read_b128 v[170:173], v151
	s_waitcnt lgkmcnt(1)
	v_lshlrev_b32_e32 v128, 16, v152
	v_and_b32_e32 v131, 0xffff0000, v152
	v_mul_f32_e32 v128, 0x42800000, v128
	v_mul_f32_e32 v131, 0x42800000, v131
	v_mov_b32_e32 v152, v129
	v_cvt_pk_fp8_f32 v152, v128, v131
	v_lshlrev_b32_e32 v168, 16, v153
	v_and_b32_e32 v131, 0xffff0000, v153
	v_mul_f32_e32 v128, 0x42800000, v168
	v_mul_f32_e32 v131, 0x42800000, v131
	v_cvt_pk_fp8_f32 v152, v128, v131 op_sel:[0,0,1]
	v_lshlrev_b32_e32 v128, 16, v154
	v_and_b32_e32 v131, 0xffff0000, v154
	v_mul_f32_e32 v128, 0x42800000, v128
	v_mul_f32_e32 v131, 0x42800000, v131
	v_mov_b32_e32 v153, v129
	v_cvt_pk_fp8_f32 v153, v128, v131
	v_lshlrev_b32_e32 v154, 16, v155
	v_and_b32_e32 v131, 0xffff0000, v155
	v_mul_f32_e32 v128, 0x42800000, v154
	v_mul_f32_e32 v131, 0x42800000, v131
	v_cvt_pk_fp8_f32 v153, v128, v131 op_sel:[0,0,1]
	s_waitcnt lgkmcnt(0)
	v_lshlrev_b32_e32 v128, 16, v170
	v_and_b32_e32 v131, 0xffff0000, v170
	v_mul_f32_e32 v128, 0x42800000, v128
	v_mul_f32_e32 v131, 0x42800000, v131
	v_mov_b32_e32 v154, v129
	v_cvt_pk_fp8_f32 v154, v128, v131
	v_lshlrev_b32_e32 v155, 16, v171
	v_and_b32_e32 v131, 0xffff0000, v171
	v_mul_f32_e32 v128, 0x42800000, v155
	v_mul_f32_e32 v131, 0x42800000, v131
	v_cvt_pk_fp8_f32 v154, v128, v131 op_sel:[0,0,1]
	v_lshlrev_b32_e32 v128, 16, v172
	v_and_b32_e32 v131, 0xffff0000, v172
	v_mul_f32_e32 v128, 0x42800000, v128
	v_mul_f32_e32 v131, 0x42800000, v131
	v_mov_b32_e32 v155, v129
	v_cvt_pk_fp8_f32 v155, v128, v131
	v_lshlrev_b32_e32 v168, 16, v173
	v_and_b32_e32 v131, 0xffff0000, v173
	v_mul_f32_e32 v128, 0x42800000, v168
	v_mul_f32_e32 v131, 0x42800000, v131
	v_cvt_pk_fp8_f32 v155, v128, v131 op_sel:[0,0,1]
	v_mad_u64_u32 v[178:179], s[22:23], s45, v164, v[132:133]
	v_mad_u64_u32 v[132:133], s[22:23], s45, v166, v[132:133]
	global_store_dwordx4 v[178:179], v[174:177], off sc1
	global_store_dwordx4 v[132:133], v[152:155], off sc1
	s_waitcnt lgkmcnt(0)
	s_andn2_b64 vcc, exec, s[20:21]
	s_cbranch_vccnz .LBB0_270
	s_add_i32 s41, s44, 0x8001
	s_cmp_ge_i32 s41, s66
	s_cbranch_scc1 .LcvwP2b_b
	s_cmpk_gt_i32 s33, 0x7ffd
	s_mov_b64 s[22:23], -1
	s_cbranch_scc0 .LBB0_282
	s_add_i32 s0, s44, 1
	s_lshr_b32 s0, s0, 9
	s_lshl_b64 s[6:7], s[0:1], 23
	s_add_u32 s6, s58, s6
	s_addc_u32 s7, s59, s7
	s_and_b32 s22, s42, 0x380
	s_lshl_b32 s20, s22, 13
	s_add_u32 s6, s6, s20
	s_addc_u32 s7, s7, 0
	s_and_b32 s23, s43, 0x7e0
	s_lshl_b32 s20, s23, 2
	s_add_u32 s20, s6, s20
	s_addc_u32 s21, s7, 0
	s_lshl_b64 s[6:7], s[0:1], 21
	s_lshl_b32 s0, s23, 10
	s_add_u32 s6, s70, s6
	s_addc_u32 s7, s71, s7
	s_add_u32 s0, s6, s0
	s_addc_u32 s7, s7, 0
	s_add_u32 s6, s0, s22
	s_addc_u32 s7, s7, 0
	s_mov_b64 s[22:23], 0
